# final norm: expert-slot load issued before the row's x/delta loads, no per-step store drain in front of the gather
# speedup vs baseline: 1.0011x; 1.0011x over previous
; #define LAS __attribute__((address_space(3)))
; __device__ __forceinline__ void phase_norm1(const Params& p, const Ctx& F, const int l) {
;     const bool fin = (l == 2), comb = (l > 0);
;     if (l == 0) { LAS float* scr = (LAS float*)(F.lds + F.wave * 16640); for (int it = F.gw; it < CV_FIRST; it += F.NGW) conv_item(p, F, scr, it, F.lane); }
;     const int b = F.gw & 7, tstride = F.NGW >> 3;
;     int cur_m = -1; f32x4 A[8], Bv[8];
;     int t = F.gw >> 3; if (fin) { while (t < CTXL) t += tstride; }
;     f32x4 vn[8], accn[8]; u32x2 dn[8]; int sn = -1;
; #pragma unroll
;     for (int j = 0; j < 8; ++j) dn[j] = (u32x2){0u, 0u};
; #pragma unroll
;     for (int j = 0; j < 8; ++j) accn[j] = (f32x4){0.f, 0.f, 0.f, 0.f};
;     if (t < TPB) { const float* xs; float* xd; row_ptrs(p, F, l, b, t, xs, xd);
; #pragma unroll
;         for (int j = 0; j < 8; ++j) vn[j] = __builtin_nontemporal_load((const f32x4*)xs + F.lane + 64 * j);
;         if (comb) {
; #pragma unroll
;             for (int j = 0; j < 8; ++j) dn[j] = __builtin_nontemporal_load((const u32x2*)(F.dlt + ((size_t)b * TPB + t) * DM + 4 * F.lane + 256 * j)); }
;         if (comb) { int s0 = -1; if (F.lane < 16) s0 = F.slot[(unsigned)((b * 16 + F.lane) * TPB + t)]; { if (fin) gather_y1(F, s0, accn); else gather_y(F, s0, accn); }
;             if (t + tstride < TPB && F.lane < 16) sn = F.slot[(unsigned)((b * 16 + F.lane) * TPB + t + tstride)]; } }
.LBB0_1457:
	s_or_b64 exec, exec, s[0:1]
	v_and_b32_e32 v32, 64, v197
	v_add_u32_e32 v32, 64, v32
	v_xor_b32_e32 v33, 1, v197
	v_cmp_lt_i32_e32 vcc, v33, v32
	v_readlane_b32 s36, v252, 17
	s_add_u32 s4, s90, 0xa00000
	v_cndmask_b32_e32 v33, v197, v33, vcc
	v_lshlrev_b32_e32 v209, 2, v33
	v_xor_b32_e32 v33, 2, v197
	v_cmp_lt_i32_e32 vcc, v33, v32
	s_mul_i32 s0, s10, 0xc000
	v_mov_b32_e32 v129, 0
	v_cndmask_b32_e32 v33, v197, v33, vcc
	v_lshlrev_b32_e32 v210, 2, v33
	v_xor_b32_e32 v33, 4, v197
	v_cmp_lt_i32_e32 vcc, v33, v32
	v_readlane_b32 s50, v252, 31
	v_readlane_b32 s51, v252, 32
	v_cndmask_b32_e32 v33, v197, v33, vcc
	v_lshlrev_b32_e32 v211, 2, v33
	v_xor_b32_e32 v33, 8, v197
	v_cmp_lt_i32_e32 vcc, v33, v32
	s_addc_u32 s5, s91, 0
	s_add_i32 s6, s0, 0x6c000
	v_cndmask_b32_e32 v33, v197, v33, vcc
	v_lshlrev_b32_e32 v212, 2, v33
	v_xor_b32_e32 v33, 16, v197
	v_cmp_lt_i32_e32 vcc, v33, v32
	v_lshl_add_u64 v[180:181], s[50:51], 0, v[128:129]
	s_mov_b64 s[0:1], 0x1000
	v_cndmask_b32_e32 v33, v197, v33, vcc
	v_lshlrev_b32_e32 v213, 2, v33
	v_xor_b32_e32 v33, 32, v197
	v_cmp_lt_i32_e32 vcc, v33, v32
	v_lshl_add_u64 v[182:183], v[180:181], 0, s[0:1]
	s_mov_b64 s[0:1], 0x1400
	v_cndmask_b32_e32 v32, v197, v33, vcc
	v_lshlrev_b32_e32 v214, 2, v32
	v_lshl_add_u64 v[184:185], v[180:181], 0, s[0:1]
	s_mov_b64 s[0:1], 0x1800
	v_lshlrev_b32_e32 v32, 1, v64
	v_mov_b32_e32 v33, v129
	s_mov_b32 s7, 0
	v_lshl_add_u64 v[186:187], v[180:181], 0, s[0:1]
	s_mov_b64 s[0:1], 0x1c00
	v_lshl_add_u64 v[190:191], s[8:9], 0, v[32:33]
	v_add_u32_e32 v32, s11, v66
	s_lshl_b32 s29, s10, 8
	v_lshl_add_u64 v[188:189], v[180:181], 0, s[0:1]
	v_cmp_gt_u32_e64 s[0:1], 16, v66
	v_mul_u32_u24_e32 v215, 0x1100, v32
	s_mov_b64 s[8:9], s[6:7]
	s_mov_b64 s[10:11], 0x10a000
	s_movk_i32 s30, 0x1000
	s_mov_b32 s12, 0x3d000000
	v_mov_b32_e32 v216, 0x358637bd
	s_mov_b32 s31, 0x800000
	v_mov_b32_e32 v148, v65
	v_readlane_b32 s37, v252, 18
	v_readlane_b32 s38, v252, 19
	v_readlane_b32 s39, v252, 20
	v_readlane_b32 s40, v252, 21
	v_readlane_b32 s41, v252, 22
	v_readlane_b32 s42, v252, 23
	v_readlane_b32 s43, v252, 24
	v_readlane_b32 s44, v252, 25
	v_readlane_b32 s45, v252, 26
	v_readlane_b32 s46, v252, 27
	v_readlane_b32 s47, v252, 28
	v_readlane_b32 s48, v252, 29
	v_readlane_b32 s49, v252, 30
	s_waitcnt vmcnt(0)
	s_branch .LBB0_1460

; __device__ __forceinline__ float bflo(unsigned w) { return __uint_as_float(w << 16); }
; __device__ __forceinline__ float bfhi(unsigned w) { return __uint_as_float(w & 0xffff0000u); }
; __device__ __forceinline__ void phase_norm1(const Params& p, const Ctx& F, const int l) {
;     ...
;         for (int j = 0; j < 8; ++j) v[j] = vn[j] + (f32x4){bflo(dn[j].x), bfhi(dn[j].x), bflo(dn[j].y), bfhi(dn[j].y)};
;         if (comb) {
;             const float* gt = F.mod + (size_t)((l - 1) * 9 + mrow) * MODW + 5 * DM;
; #pragma unroll
;             for (int j = 0; j < 8; ++j) { v[j] += *((const f32x4*)gt + F.lane + 64 * j) * accn[j] * (1.f / Y_SCALE); if (!fin) *((f32x4*)xd + F.lane + 64 * j) = v[j]; }
;         }
;         { const int t2 = t + tstride;
;           if (t2 < TPB) { const float* xs2; float* xd2; row_ptrs(p, F, l, b, t2, xs2, xd2);
; #pragma unroll
;             for (int j = 0; j < 8; ++j) vn[j] = __builtin_nontemporal_load((const f32x4*)xs2 + F.lane + 64 * j);
;             if (comb) {
; #pragma unroll
;                 for (int j = 0; j < 8; ++j) dn[j] = __builtin_nontemporal_load((const u32x2*)(F.dlt + ((size_t)b * TPB + t2) * DM + 4 * F.lane + 256 * j)); }
;             if (comb) { { if (fin) gather_y1(F, sn, accn); else gather_y(F, sn, accn); } const int t3 = t2 + tstride; sn = -1; if (t3 < TPB && F.lane < 16) sn = F.slot[(unsigned)((b * 16 + F.lane) * TPB + t3)]; } } }
;         if (mrow != cur_m) { cur_m = mrow;
;             if (!fin) {
;                 const float* mr = F.mod + (size_t)(l * 9 + mrow) * MODW;
; #pragma unroll
;                 for (int j = 0; j < 8; ++j) { const f32x4 g = *((const f32x4*)(p.g_mix + l * DM) + F.lane + 64 * j), sc = *((const f32x4*)(mr + DM) + F.lane + 64 * j);
;                     A[j] = g * (sc + 1.f); Bv[j] = *((const f32x4*)mr + F.lane + 64 * j); }
;             }
;         }
;         float ss = 0.f;
; #pragma unroll
;         for (int j = 0; j < 8; ++j) ss += (v[j].x * v[j].x + v[j].y * v[j].y) + (v[j].z * v[j].z + v[j].w * v[j].w);
;         const float rstd = rsqrtf(wave_sum(ss) * (1.f / DM) + EPS);
.LBB0_1459:
	v_lshlrev_b32_e32 v96, 16, v146
	v_and_b32_e32 v97, 0xffff0000, v146
	v_lshlrev_b32_e32 v98, 16, v147
	v_and_b32_e32 v99, 0xffff0000, v147
	v_pk_add_f32 v[28:29], v[28:29], v[96:97]
	v_pk_add_f32 v[30:31], v[30:31], v[98:99]
	v_lshlrev_b32_e32 v96, 16, v144
	v_and_b32_e32 v97, 0xffff0000, v144
	v_lshlrev_b32_e32 v98, 16, v145
	v_and_b32_e32 v99, 0xffff0000, v145
	v_pk_add_f32 v[24:25], v[24:25], v[96:97]
	v_pk_add_f32 v[26:27], v[26:27], v[98:99]
	v_lshlrev_b32_e32 v96, 16, v142
	v_and_b32_e32 v97, 0xffff0000, v142
	v_lshlrev_b32_e32 v98, 16, v143
	v_and_b32_e32 v99, 0xffff0000, v143
	v_pk_add_f32 v[20:21], v[20:21], v[96:97]
	v_pk_add_f32 v[22:23], v[22:23], v[98:99]
	v_lshlrev_b32_e32 v96, 16, v140
	v_and_b32_e32 v97, 0xffff0000, v140
	v_lshlrev_b32_e32 v98, 16, v141
	v_and_b32_e32 v99, 0xffff0000, v141
	v_pk_add_f32 v[16:17], v[16:17], v[96:97]
	v_pk_add_f32 v[18:19], v[18:19], v[98:99]
	v_lshlrev_b32_e32 v96, 16, v138
	v_and_b32_e32 v97, 0xffff0000, v138
	v_lshlrev_b32_e32 v98, 16, v139
	v_and_b32_e32 v99, 0xffff0000, v139
	v_pk_add_f32 v[12:13], v[12:13], v[96:97]
	v_pk_add_f32 v[14:15], v[14:15], v[98:99]
	v_lshlrev_b32_e32 v96, 16, v136
	v_and_b32_e32 v97, 0xffff0000, v136
	v_lshlrev_b32_e32 v98, 16, v137
	v_and_b32_e32 v99, 0xffff0000, v137
	v_pk_add_f32 v[96:97], v[8:9], v[96:97]
	v_pk_add_f32 v[8:9], v[10:11], v[98:99]
	v_lshlrev_b32_e32 v10, 16, v134
	v_and_b32_e32 v11, 0xffff0000, v134
	v_lshlrev_b32_e32 v98, 16, v135
	v_and_b32_e32 v99, 0xffff0000, v135
	v_pk_add_f32 v[100:101], v[4:5], v[10:11]
	v_lshlrev_b32_e32 v4, 16, v132
	v_and_b32_e32 v5, 0xffff0000, v132
	v_pk_add_f32 v[98:99], v[6:7], v[98:99]
	v_lshlrev_b32_e32 v6, 16, v133
	v_and_b32_e32 v7, 0xffff0000, v133
	v_pk_add_f32 v[102:103], v[0:1], v[4:5]
	s_waitcnt vmcnt(5)
	v_pk_mul_f32 v[0:1], v[154:155], v[94:95]
	v_pk_add_f32 v[104:105], v[2:3], v[6:7]
	v_pk_mul_f32 v[2:3], v[148:149], v[92:93]
	v_pk_fma_f32 v[30:31], v[0:1], s[12:13], v[30:31] op_sel_hi:[1,0,1]
	v_pk_mul_f32 v[0:1], v[156:157], v[90:91]
	v_pk_fma_f32 v[28:29], v[2:3], s[12:13], v[28:29] op_sel_hi:[1,0,1]
	v_pk_mul_f32 v[2:3], v[150:151], v[88:89]
	v_pk_fma_f32 v[26:27], v[0:1], s[12:13], v[26:27] op_sel_hi:[1,0,1]
	v_pk_mul_f32 v[0:1], v[160:161], v[86:87]
	v_pk_fma_f32 v[24:25], v[2:3], s[12:13], v[24:25] op_sel_hi:[1,0,1]
	v_pk_mul_f32 v[2:3], v[152:153], v[84:85]
	v_pk_fma_f32 v[22:23], v[0:1], s[12:13], v[22:23] op_sel_hi:[1,0,1]
	s_waitcnt vmcnt(4)
	v_pk_mul_f32 v[0:1], v[164:165], v[82:83]
	v_pk_fma_f32 v[20:21], v[2:3], s[12:13], v[20:21] op_sel_hi:[1,0,1]
	v_pk_mul_f32 v[2:3], v[158:159], v[80:81]
	v_pk_fma_f32 v[18:19], v[0:1], s[12:13], v[18:19] op_sel_hi:[1,0,1]
	s_waitcnt vmcnt(3)
	v_pk_mul_f32 v[0:1], v[168:169], v[78:79]
	v_pk_fma_f32 v[16:17], v[2:3], s[12:13], v[16:17] op_sel_hi:[1,0,1]
	v_pk_mul_f32 v[2:3], v[162:163], v[76:77]
	v_pk_fma_f32 v[4:5], v[0:1], s[12:13], v[14:15] op_sel_hi:[1,0,1]
	s_waitcnt vmcnt(0)
	s_add_i32 s6, s26, s13
	s_cmpk_lt_i32 s6, 0x1100
	s_cselect_b64 s[24:25], -1, 0
	s_and_b64 s[24:25], s[24:25], s[0:1]
	v_cndmask_b32_e64 v208, -1, v250, s[24:25]
	v_pk_mul_f32 v[14:15], v[174:175], v[64:65]
	v_pk_fma_f32 v[6:7], v[2:3], s[12:13], v[12:13] op_sel_hi:[1,0,1]
	v_pk_mul_f32 v[2:3], v[166:167], v[72:73]
	v_pk_mul_f32 v[12:13], v[178:179], v[66:67]
	v_pk_fma_f32 v[66:67], v[14:15], s[12:13], v[102:103] op_sel_hi:[1,0,1]
	v_mov_b32_e32 v14, v29
	v_mov_b32_e32 v15, v25
	v_pk_fma_f32 v[10:11], v[2:3], s[12:13], v[96:97] op_sel_hi:[1,0,1]
	v_pk_mul_f32 v[2:3], v[170:171], v[68:69]
	v_pk_fma_f32 v[64:65], v[12:13], s[12:13], v[104:105] op_sel_hi:[1,0,1]
	v_mov_b32_e32 v12, v28
	v_mov_b32_e32 v13, v24
	v_pk_mul_f32 v[14:15], v[14:15], v[14:15]
	v_mov_b32_e32 v68, v31
	v_mov_b32_e32 v69, v27
	v_pk_fma_f32 v[12:13], v[12:13], v[12:13], v[14:15]
	v_mov_b32_e32 v14, v30
	v_mov_b32_e32 v15, v26
	v_pk_mul_f32 v[68:69], v[68:69], v[68:69]
	v_pk_mul_f32 v[0:1], v[172:173], v[74:75]
	v_pk_fma_f32 v[14:15], v[14:15], v[14:15], v[68:69]
	v_pk_mul_f32 v[68:69], v[20:21], v[20:21]
	v_pk_add_f32 v[12:13], v[12:13], v[14:15]
	v_pk_mul_f32 v[14:15], v[22:23], v[22:23]
	v_pk_fma_f32 v[8:9], v[0:1], s[12:13], v[8:9] op_sel_hi:[1,0,1]
	v_pk_mul_f32 v[0:1], v[176:177], v[70:71]
	v_pk_mov_b32 v[70:71], v[68:69], v[14:15] op_sel:[1,0]
	v_mov_b32_e32 v69, v15
	v_pk_add_f32 v[14:15], v[70:71], v[68:69]
	v_mul_f32_e32 v68, v6, v6
	v_mul_f32_e32 v69, v7, v7
	v_pk_add_f32 v[12:13], v[12:13], v[12:13] op_sel:[0,1] op_sel_hi:[1,0]
	v_pk_add_f32 v[14:15], v[14:15], v[14:15] op_sel:[0,1] op_sel_hi:[1,0]
	v_mov_b32_e32 v13, v68
	v_mov_b32_e32 v15, v69
	v_pk_add_f32 v[68:69], v[12:13], v[14:15]
	global_load_dwordx4 v[12:15], v[180:181], off
	global_load_dwordx4 v[76:79], v[180:181], off offset:1024
	global_load_dwordx4 v[80:83], v[180:181], off offset:2048
	global_load_dwordx4 v[84:87], v[180:181], off offset:3072
	global_load_dwordx4 v[88:91], v[182:183], off
	global_load_dwordx4 v[92:95], v[184:185], off
	global_load_dwordx4 v[108:111], v[186:187], off
	global_load_dwordx4 v[112:115], v[188:189], off
	v_mul_f32_e32 v70, v17, v17
	v_mul_f32_e32 v72, v4, v4
	v_pk_fma_f32 v[70:71], v[16:17], v[16:17], v[70:71] op_sel_hi:[1,1,0]
	v_mul_f32_e32 v74, v5, v5
	v_mov_b32_e32 v71, v72
	v_mul_f32_e32 v72, v19, v19
	v_pk_fma_f32 v[72:73], v[18:19], v[18:19], v[72:73] op_sel_hi:[1,1,0]
	v_pk_fma_f32 v[0:1], v[0:1], s[12:13], v[98:99] op_sel_hi:[1,0,1]
	v_mov_b32_e32 v73, v74
	v_pk_add_f32 v[70:71], v[70:71], v[72:73]
	v_pk_mul_f32 v[72:73], v[10:11], v[10:11]
	v_pk_add_f32 v[68:69], v[68:69], v[70:71]
	v_pk_mul_f32 v[70:71], v[8:9], v[8:9]
	v_pk_add_f32 v[68:69], v[68:69], v[68:69] op_sel:[0,1] op_sel_hi:[1,0]
	v_pk_mov_b32 v[74:75], v[72:73], v[70:71] op_sel:[1,0]
	v_mov_b32_e32 v73, v71
	v_pk_add_f32 v[70:71], v[74:75], v[72:73]
	v_mul_f32_e32 v72, v66, v66
	v_mul_f32_e32 v73, v67, v67
	v_pk_add_f32 v[70:71], v[70:71], v[70:71] op_sel:[0,1] op_sel_hi:[1,0]
	v_pk_fma_f32 v[2:3], v[2:3], s[12:13], v[100:101] op_sel_hi:[1,0,1]
	v_mov_b32_e32 v69, v72
	v_mov_b32_e32 v71, v73
	v_pk_add_f32 v[68:69], v[68:69], v[70:71]
	v_mul_f32_e32 v70, v3, v3
	v_mul_f32_e32 v72, v1, v1
	v_mul_f32_e32 v74, v64, v64
	v_mul_f32_e32 v75, v65, v65
	v_pk_fma_f32 v[70:71], v[2:3], v[2:3], v[70:71] op_sel_hi:[1,1,0]
	v_pk_fma_f32 v[72:73], v[0:1], v[0:1], v[72:73] op_sel_hi:[1,1,0]
	v_mov_b32_e32 v71, v74
	v_mov_b32_e32 v73, v75
	v_pk_add_f32 v[70:71], v[70:71], v[72:73]
	s_lshl_b64 s[16:17], s[16:17], 13
	v_pk_add_f32 v[68:69], v[68:69], v[70:71]
	s_add_u32 s16, s18, s16
	v_add_f32_e32 v68, v68, v69
	ds_bpermute_b32 v69, v209, v68
	s_addc_u32 s17, s19, s17
	v_mov_b64_e32 v[132:133], v[206:207]
	v_mov_b64_e32 v[134:135], v[204:205]
	v_mov_b64_e32 v[136:137], v[202:203]
	s_waitcnt lgkmcnt(0)
; __device__ __forceinline__ void phase_norm1(const Params& p, const Ctx& F, const int l) {
;     ...
;         const float rstd = rsqrtf(wave_sum(ss) * (1.f / DM) + EPS);
;         if (fin) {
; #pragma unroll
;             for (int j = 0; j < 8; ++j) __builtin_nontemporal_store(v[j] * rstd * *((const f32x4*)p.g_final + F.lane + 64 * j), (f32x4*)xd + F.lane + 64 * j);
	v_add_f32_e32 v68, v68, v69
	ds_bpermute_b32 v69, v210, v68
	v_mov_b64_e32 v[138:139], v[200:201]
	v_mov_b64_e32 v[140:141], v[198:199]
	v_mov_b64_e32 v[142:143], v[196:197]
	v_mov_b64_e32 v[144:145], v[194:195]
	s_waitcnt lgkmcnt(0)
	v_add_f32_e32 v68, v68, v69
	ds_bpermute_b32 v69, v211, v68
	v_mov_b64_e32 v[146:147], v[192:193]
	v_mov_b32_e32 v148, v217
	v_mov_b32_e32 v149, v218
	v_mov_b32_e32 v154, v219
	s_waitcnt lgkmcnt(0)
	v_add_f32_e32 v68, v68, v69
	ds_bpermute_b32 v69, v212, v68
	v_mov_b32_e32 v155, v220
	v_mov_b32_e32 v150, v221
	v_mov_b32_e32 v151, v222
	v_mov_b32_e32 v156, v223
	s_waitcnt lgkmcnt(0)
	v_add_f32_e32 v68, v68, v69
	ds_bpermute_b32 v69, v213, v68
	v_mov_b32_e32 v157, v224
	v_mov_b32_e32 v152, v225
	v_mov_b32_e32 v153, v226
	v_mov_b32_e32 v160, v227
	s_waitcnt lgkmcnt(0)
	v_add_f32_e32 v68, v68, v69
	ds_bpermute_b32 v69, v214, v68
	v_mov_b32_e32 v161, v228
	v_mov_b32_e32 v158, v229
	v_mov_b32_e32 v159, v230
	v_mov_b32_e32 v164, v231
	s_waitcnt lgkmcnt(0)
	v_add_f32_e32 v68, v68, v69
	v_fmamk_f32 v68, v68, 0x3a000000, v216
	v_mul_f32_e32 v69, 0x4b800000, v68
	v_cmp_gt_f32_e32 vcc, s31, v68
	v_mov_b32_e32 v165, v232
	v_mov_b32_e32 v162, v233
	v_cndmask_b32_e32 v68, v68, v69, vcc
	v_rsq_f32_e32 v68, v68
	v_mov_b32_e32 v163, v235
	v_mov_b32_e32 v168, v236
	v_mov_b32_e32 v169, v237
	v_mul_f32_e32 v69, 0x45800000, v68
	v_cndmask_b32_e32 v72, v68, v69, vcc
	v_pk_mul_f32 v[28:29], v[28:29], v[72:73] op_sel_hi:[1,0]
	v_pk_mul_f32 v[30:31], v[30:31], v[72:73] op_sel_hi:[1,0]
	s_waitcnt vmcnt(0)
	v_pk_mul_f32 v[12:13], v[12:13], v[28:29]
	v_pk_mul_f32 v[14:15], v[14:15], v[30:31]
	global_store_dwordx4 v128, v[12:15], s[16:17] nt
	v_pk_mul_f32 v[26:27], v[26:27], v[72:73] op_sel_hi:[1,0]
	v_pk_mul_f32 v[24:25], v[24:25], v[72:73] op_sel_hi:[1,0]
	v_pk_mul_f32 v[22:23], v[22:23], v[72:73] op_sel_hi:[1,0]
	v_pk_mul_f32 v[20:21], v[20:21], v[72:73] op_sel_hi:[1,0]
	v_pk_mul_f32 v[18:19], v[18:19], v[72:73] op_sel_hi:[1,0]
	v_pk_mul_f32 v[16:17], v[16:17], v[72:73] op_sel_hi:[1,0]
	v_pk_mul_f32 v[8:9], v[8:9], v[72:73] op_sel_hi:[1,0]
	v_pk_mul_f32 v[10:11], v[10:11], v[72:73] op_sel_hi:[1,0]
	v_mov_b64_e32 v[28:29], v[32:33]
	v_mov_b64_e32 v[30:31], v[34:35]
	v_pk_mul_f32 v[34:35], v[64:65], v[72:73] op_sel_hi:[1,0]
	v_pk_mul_f32 v[32:33], v[66:67], v[72:73] op_sel_hi:[1,0]
	v_mov_b32_e32 v166, v238
	v_mov_b32_e32 v167, v239
	v_mov_b32_e32 v172, v240
	v_mov_b32_e32 v173, v241
	v_mov_b32_e32 v170, v242
	v_mov_b32_e32 v171, v243
	v_mov_b32_e32 v176, v244
	v_mov_b32_e32 v177, v245
	v_mov_b32_e32 v174, v246
	v_mov_b32_e32 v175, v247
	v_mov_b32_e32 v178, v248
	v_mov_b32_e32 v179, v234
	v_pk_mul_f32 v[76:77], v[76:77], v[24:25]
	v_pk_mul_f32 v[78:79], v[78:79], v[26:27]
	global_store_dwordx4 v128, v[76:79], s[16:17] offset:1024 nt
	v_mov_b64_e32 v[24:25], v[36:37]
	v_mov_b64_e32 v[26:27], v[38:39]
	v_pk_mul_f32 v[80:81], v[80:81], v[20:21]
	v_pk_mul_f32 v[82:83], v[82:83], v[22:23]
	global_store_dwordx4 v128, v[80:83], s[16:17] offset:2048 nt
	v_mov_b64_e32 v[20:21], v[40:41]
	v_mov_b64_e32 v[22:23], v[42:43]
	v_pk_mul_f32 v[84:85], v[84:85], v[16:17]
	v_pk_mul_f32 v[86:87], v[86:87], v[18:19]
	global_store_dwordx4 v128, v[84:87], s[16:17] offset:3072 nt
	v_lshl_add_u64 v[16:17], s[16:17], 0, v[128:129]
	v_add_co_u32_e32 v74, vcc, s30, v16
	s_nop 1
	v_addc_co_u32_e32 v75, vcc, 0, v17, vcc
	v_pk_mul_f32 v[16:17], v[4:5], v[72:73] op_sel_hi:[1,0]
	v_pk_mul_f32 v[4:5], v[6:7], v[72:73] op_sel_hi:[1,0]
	s_andn2_b64 vcc, exec, s[14:15]
	v_pk_mul_f32 v[4:5], v[88:89], v[4:5]
	v_pk_mul_f32 v[6:7], v[90:91], v[16:17]
	global_store_dwordx4 v[74:75], v[4:7], off nt
	v_mov_b64_e32 v[12:13], v[48:49]
	v_mov_b64_e32 v[16:17], v[44:45]
	v_mov_b64_e32 v[14:15], v[50:51]
	v_mov_b64_e32 v[18:19], v[46:47]
	v_pk_mul_f32 v[4:5], v[92:93], v[10:11]
	v_pk_mul_f32 v[6:7], v[94:95], v[8:9]
	global_store_dwordx4 v[74:75], v[4:7], off offset:1024 nt
	v_pk_mul_f32 v[8:9], v[0:1], v[72:73] op_sel_hi:[1,0]
	v_pk_mul_f32 v[0:1], v[2:3], v[72:73] op_sel_hi:[1,0]
	v_pk_mul_f32 v[2:3], v[8:9], v[110:111]
	v_pk_mul_f32 v[0:1], v[0:1], v[108:109]
	global_store_dwordx4 v[74:75], v[0:3], off offset:2048 nt
	s_nop 1
	v_mov_b64_e32 v[4:5], v[56:57]
	v_mov_b64_e32 v[0:1], v[60:61]
	v_mov_b64_e32 v[8:9], v[52:53]
	v_mov_b64_e32 v[2:3], v[62:63]
	v_mov_b64_e32 v[6:7], v[58:59]
	v_mov_b64_e32 v[10:11], v[54:55]
	v_pk_mul_f32 v[32:33], v[32:33], v[112:113]
	v_pk_mul_f32 v[34:35], v[34:35], v[114:115]
	global_store_dwordx4 v[74:75], v[32:35], off offset:3072 nt
	s_cbranch_vccz .LBB0_1478

; __device__ __forceinline__ void gather_y1(const Ctx& F, const int s, f32x4 (&acc)[8]) {
; #pragma unroll
;     for (int j = 0; j < 8; ++j) acc[j] = (f32x4){0.f, 0.f, 0.f, 0.f};
; __device__ __forceinline__ void phase_norm1(const Params& p, const Ctx& F, const int l) {
;     ...
;         { const int t2 = t + tstride;
;           if (t2 < TPB) { const float* xs2; float* xd2; row_ptrs(p, F, l, b, t2, xs2, xd2);
; #pragma unroll
;             for (int j = 0; j < 8; ++j) vn[j] = __builtin_nontemporal_load((const f32x4*)xs2 + F.lane + 64 * j);
;             if (comb) {
; #pragma unroll
;                 for (int j = 0; j < 8; ++j) dn[j] = __builtin_nontemporal_load((const u32x2*)(F.dlt + ((size_t)b * TPB + t2) * DM + 4 * F.lane + 256 * j)); }
;             if (comb) { { if (fin) gather_y1(F, sn, accn); else gather_y(F, sn, accn); } const int t3 = t2 + tstride; sn = -1; if (t3 < TPB && F.lane < 16) sn = F.slot[(unsigned)((b * 16 + F.lane) * TPB + t3)]; } } }
.LBB0_1469:
	s_add_i32 s6, s26, s13
	s_cmpk_lt_i32 s6, 0x1100
	s_cselect_b64 s[24:25], -1, 0
	s_and_b64 s[24:25], s[24:25], s[0:1]
	v_add_u32_e32 v96, s6, v215
	v_cndmask_b32_e64 v96, 0, v96, s[24:25]
	v_mov_b32_e32 v97, v129
	v_lshl_add_u64 v[96:97], v[96:97], 2, s[2:3]
	global_load_dword v250, v[96:97], off
	s_lshl_b64 s[20:21], s[20:21], 13
	s_add_u32 s20, s22, s20
	s_addc_u32 s21, s23, s21
	v_lshl_add_u64 v[48:49], s[20:21], 0, v[128:129]
	global_load_dwordx4 v[32:35], v128, s[20:21] nt
	global_load_dwordx4 v[36:39], v128, s[20:21] offset:1024 nt
	global_load_dwordx4 v[40:43], v128, s[20:21] offset:2048 nt
	global_load_dwordx4 v[44:47], v128, s[20:21] offset:3072 nt
	s_add_u32 s20, s26, s28
	s_addc_u32 s21, s33, 0
	v_add_co_u32_e32 v60, vcc, s30, v48
	s_lshl_b64 s[20:21], s[20:21], 12
	s_nop 0
	v_addc_co_u32_e32 v61, vcc, 0, v49, vcc
	v_lshl_add_u64 v[96:97], v[190:191], 0, s[20:21]
	global_load_dwordx4 v[48:51], v[60:61], off nt
	global_load_dwordx4 v[52:55], v[60:61], off offset:1024 nt
	global_load_dwordx4 v[56:59], v[60:61], off offset:2048 nt
	s_nop 0
	global_load_dwordx4 v[60:63], v[60:61], off offset:3072 nt
	s_nop 0
	global_load_dwordx2 v[192:193], v[96:97], off nt
	global_load_dwordx2 v[194:195], v[96:97], off offset:512 nt
	global_load_dwordx2 v[196:197], v[96:97], off offset:1024 nt
	global_load_dwordx2 v[198:199], v[96:97], off offset:1536 nt
	global_load_dwordx2 v[200:201], v[96:97], off offset:2048 nt
	global_load_dwordx2 v[202:203], v[96:97], off offset:2560 nt
	global_load_dwordx2 v[204:205], v[96:97], off offset:3072 nt
	global_load_dwordx2 v[206:207], v[96:97], off offset:3584 nt
	v_mov_b32_e32 v98, v129
	v_mov_b32_e32 v99, v129
	v_mov_b32_e32 v96, v129
	v_mov_b32_e32 v97, v129
	v_mov_b64_e32 v[102:103], v[98:99]
	v_mov_b64_e32 v[106:107], v[98:99]
	v_mov_b64_e32 v[110:111], v[98:99]
	v_mov_b64_e32 v[114:115], v[98:99]
	v_mov_b64_e32 v[118:119], v[98:99]
	v_mov_b64_e32 v[122:123], v[98:99]
	v_mov_b64_e32 v[126:127], v[98:99]
	s_mov_b32 s20, 0
	v_mov_b32_e32 v217, 0
	v_mov_b64_e32 v[100:101], v[96:97]
	v_mov_b64_e32 v[104:105], v[96:97]
	v_mov_b64_e32 v[108:109], v[96:97]
	v_mov_b64_e32 v[112:113], v[96:97]
	v_mov_b64_e32 v[116:117], v[96:97]
	v_mov_b64_e32 v[120:121], v[96:97]
	v_mov_b64_e32 v[124:125], v[96:97]
	v_mov_b32_e32 v218, 0
	v_mov_b32_e32 v219, 0
	v_mov_b32_e32 v220, 0
	v_mov_b32_e32 v221, 0
	v_mov_b32_e32 v222, 0
	v_mov_b32_e32 v223, 0
	v_mov_b32_e32 v224, 0
	v_mov_b32_e32 v225, 0
	v_mov_b32_e32 v226, 0
	v_mov_b32_e32 v227, 0
	v_mov_b32_e32 v228, 0
	v_mov_b32_e32 v229, 0
	v_mov_b32_e32 v230, 0
	v_mov_b32_e32 v231, 0
	v_mov_b32_e32 v232, 0
	v_mov_b32_e32 v233, 0
	v_mov_b32_e32 v235, 0
	v_mov_b32_e32 v236, 0
	v_mov_b32_e32 v237, 0
	v_mov_b32_e32 v238, 0
	v_mov_b32_e32 v239, 0
	v_mov_b32_e32 v240, 0
	v_mov_b32_e32 v241, 0
	v_mov_b32_e32 v242, 0
	v_mov_b32_e32 v243, 0
	v_mov_b32_e32 v244, 0
	v_mov_b32_e32 v245, 0
	v_mov_b32_e32 v246, 0
	v_mov_b32_e32 v247, 0
	v_mov_b32_e32 v248, 0
	v_mov_b32_e32 v234, 0
	s_branch .LBB0_1471

; __device__ __forceinline__ f32x4 unpack_f8x4(unsigned w) { const auto lo = __builtin_amdgcn_cvt_pk_f32_fp8((int)w, false), hi = __builtin_amdgcn_cvt_pk_f32_fp8((int)w, true); return (f32x4){lo[0], lo[1], hi[0], hi[1]}; }
; __device__ __forceinline__ void gather_y1(const Ctx& F, const int s, f32x4 (&acc)[8]) {
;     ...
;     for (int e = 0; e < 16; ++e) { const int se = __builtin_amdgcn_readlane(s, e);
;         if (se >= 0) { const unsigned char* yr = F.y8 + (size_t)se * DM + 4 * F.lane;
; #pragma unroll
;             for (int j = 0; j < 8; ++j) { const unsigned w = __builtin_nontemporal_load((const unsigned*)(yr + 256 * j)); acc[j] += unpack_f8x4(w); } } }
.LBB0_1471:
	v_readlane_b32 s6, v208, s20
	s_cmp_lt_i32 s6, 0
	s_cbranch_scc1 .LBB0_1473
	s_lshl_b64 s[22:23], s[6:7], 11
	v_lshl_add_u64 v[218:219], v[130:131], 0, s[22:23]
	global_load_dword v217, v[218:219], off nt
	global_load_dword v224, v[218:219], off offset:256 nt
	global_load_dword v228, v[218:219], off offset:512 nt
	global_load_dword v232, v[218:219], off offset:768 nt
	global_load_dword v236, v[218:219], off offset:1024 nt
	global_load_dword v240, v[218:219], off offset:1280 nt
	global_load_dword v244, v[218:219], off offset:1536 nt
	global_load_dword v248, v[218:219], off offset:1792 nt
	s_waitcnt vmcnt(7)
	v_cvt_pk_f32_fp8_e32 v[218:219], v217
	v_cvt_pk_f32_fp8_sdwa v[220:221], v217 src0_sel:WORD_1
	s_waitcnt vmcnt(6)
	v_cvt_pk_f32_fp8_e32 v[222:223], v224
	v_cvt_pk_f32_fp8_sdwa v[224:225], v224 src0_sel:WORD_1
	s_waitcnt vmcnt(5)
	v_cvt_pk_f32_fp8_e32 v[226:227], v228
	v_cvt_pk_f32_fp8_sdwa v[228:229], v228 src0_sel:WORD_1
	s_waitcnt vmcnt(4)
	v_cvt_pk_f32_fp8_e32 v[230:231], v232
	v_cvt_pk_f32_fp8_sdwa v[232:233], v232 src0_sel:WORD_1
	s_waitcnt vmcnt(3)
	v_cvt_pk_f32_fp8_e32 v[234:235], v236
	v_cvt_pk_f32_fp8_sdwa v[236:237], v236 src0_sel:WORD_1
	s_waitcnt vmcnt(2)
	v_cvt_pk_f32_fp8_e32 v[238:239], v240
	v_cvt_pk_f32_fp8_sdwa v[240:241], v240 src0_sel:WORD_1
	s_waitcnt vmcnt(1)
	v_cvt_pk_f32_fp8_e32 v[242:243], v244
	v_cvt_pk_f32_fp8_sdwa v[244:245], v244 src0_sel:WORD_1
	s_waitcnt vmcnt(0)
	v_cvt_pk_f32_fp8_e32 v[246:247], v248
	v_cvt_pk_f32_fp8_sdwa v[248:249], v248 src0_sel:WORD_1
	v_pk_add_f32 v[126:127], v[126:127], v[220:221]
	v_pk_add_f32 v[124:125], v[124:125], v[218:219]
	v_pk_add_f32 v[122:123], v[122:123], v[224:225]
	v_pk_add_f32 v[120:121], v[120:121], v[222:223]
	v_pk_add_f32 v[118:119], v[118:119], v[228:229]
	v_pk_add_f32 v[116:117], v[116:117], v[226:227]
	v_pk_add_f32 v[114:115], v[114:115], v[232:233]
	v_pk_add_f32 v[112:113], v[112:113], v[230:231]
	v_pk_add_f32 v[110:111], v[110:111], v[236:237]
	v_pk_add_f32 v[108:109], v[108:109], v[234:235]
	v_pk_add_f32 v[106:107], v[106:107], v[240:241]
	v_pk_add_f32 v[104:105], v[104:105], v[238:239]
	v_pk_add_f32 v[102:103], v[102:103], v[244:245]
	v_pk_add_f32 v[100:101], v[100:101], v[242:243]
	v_pk_add_f32 v[98:99], v[98:99], v[248:249]
	v_pk_add_f32 v[96:97], v[96:97], v[246:247]
	v_mov_b32_e32 v217, v124
	v_mov_b32_e32 v218, v125
	v_mov_b32_e32 v219, v126
	v_mov_b32_e32 v220, v127
	v_mov_b32_e32 v221, v120
	v_mov_b32_e32 v222, v121
	v_mov_b32_e32 v223, v122
	v_mov_b32_e32 v224, v123
	v_mov_b32_e32 v225, v116
	v_mov_b32_e32 v226, v117
	v_mov_b32_e32 v227, v118
	v_mov_b32_e32 v228, v119
	v_mov_b32_e32 v229, v112
	v_mov_b32_e32 v230, v113
	v_mov_b32_e32 v231, v114
	v_mov_b32_e32 v232, v115
	v_mov_b32_e32 v233, v108
	v_mov_b32_e32 v235, v109
	v_mov_b32_e32 v236, v110
	v_mov_b32_e32 v237, v111
	v_mov_b32_e32 v238, v104
	v_mov_b32_e32 v239, v105
	v_mov_b32_e32 v240, v106
	v_mov_b32_e32 v241, v107
	v_mov_b32_e32 v242, v100
	v_mov_b32_e32 v243, v101
	v_mov_b32_e32 v244, v102
	v_mov_b32_e32 v245, v103
	v_mov_b32_e32 v246, v96
	v_mov_b32_e32 v247, v97
	v_mov_b32_e32 v248, v98
	v_mov_b32_e32 v234, v99

; __device__ __forceinline__ void phase_norm1(const Params& p, const Ctx& F, const int l) {
;     ...
;         { const int t2 = t + tstride;
;           if (t2 < TPB) { const float* xs2; float* xd2; row_ptrs(p, F, l, b, t2, xs2, xd2);
; #pragma unroll
;             for (int j = 0; j < 8; ++j) vn[j] = __builtin_nontemporal_load((const f32x4*)xs2 + F.lane + 64 * j);
;             if (comb) {
; #pragma unroll
;                 for (int j = 0; j < 8; ++j) dn[j] = __builtin_nontemporal_load((const u32x2*)(F.dlt + ((size_t)b * TPB + t2) * DM + 4 * F.lane + 256 * j)); }
;             if (comb) { { if (fin) gather_y1(F, sn, accn); else gather_y(F, sn, accn); } const int t3 = t2 + tstride; sn = -1; if (t3 < TPB && F.lane < 16) sn = F.slot[(unsigned)((b * 16 + F.lane) * TPB + t3)]; } } }
.LBB0_1475:
	v_mov_b64_e32 v[34:35], v[30:31]
	v_mov_b64_e32 v[38:39], v[26:27]
	v_mov_b64_e32 v[42:43], v[22:23]
	v_mov_b64_e32 v[46:47], v[18:19]
	v_mov_b64_e32 v[50:51], v[14:15]
	v_mov_b64_e32 v[54:55], v[10:11]
	v_mov_b64_e32 v[58:59], v[6:7]
	v_mov_b64_e32 v[62:63], v[2:3]
	v_mov_b32_e32 v234, v179
	v_mov_b32_e32 v248, v178
	v_mov_b32_e32 v247, v175
	v_mov_b32_e32 v246, v174
	v_mov_b32_e32 v245, v177
	v_mov_b32_e32 v244, v176
	v_mov_b32_e32 v243, v171
	v_mov_b32_e32 v242, v170
	v_mov_b32_e32 v241, v173
	v_mov_b32_e32 v240, v172
	v_mov_b32_e32 v239, v167
	v_mov_b32_e32 v238, v166
	v_mov_b32_e32 v237, v169
	v_mov_b32_e32 v236, v168
	v_mov_b32_e32 v235, v163
	v_mov_b32_e32 v233, v162
	v_mov_b32_e32 v232, v165
	v_mov_b32_e32 v231, v164
	v_mov_b32_e32 v230, v159
	v_mov_b32_e32 v229, v158
	v_mov_b32_e32 v228, v161
	v_mov_b32_e32 v227, v160
	v_mov_b32_e32 v226, v153
	v_mov_b32_e32 v225, v152
	v_mov_b32_e32 v224, v157
	v_mov_b32_e32 v223, v156
	v_mov_b32_e32 v222, v151
	v_mov_b32_e32 v221, v150
	v_mov_b32_e32 v220, v155
	v_mov_b32_e32 v219, v154
	v_mov_b32_e32 v218, v149
	v_mov_b32_e32 v217, v148
	v_mov_b64_e32 v[192:193], v[146:147]
	v_mov_b64_e32 v[194:195], v[144:145]
	v_mov_b64_e32 v[196:197], v[142:143]
	v_mov_b64_e32 v[198:199], v[140:141]
	v_mov_b64_e32 v[200:201], v[138:139]
	v_mov_b64_e32 v[202:203], v[136:137]
	v_mov_b64_e32 v[204:205], v[134:135]
	v_mov_b64_e32 v[206:207], v[132:133]
	v_mov_b64_e32 v[32:33], v[28:29]
	v_mov_b64_e32 v[36:37], v[24:25]
	v_mov_b64_e32 v[40:41], v[20:21]
	v_mov_b64_e32 v[44:45], v[16:17]
	v_mov_b64_e32 v[48:49], v[12:13]
	v_mov_b64_e32 v[52:53], v[8:9]
	v_mov_b64_e32 v[56:57], v[4:5]
	v_mov_b64_e32 v[60:61], v[0:1]
	s_branch .LBB0_1459
.LBB0_1476:
	s_branch .LBB0_1459
.LBB0_1478:
	s_endpgm
